# P2 states: next head's conv pieces+weights requested one head further ahead (second register set); P5: mid-head vmcnt(0) replaced by a counted wait at the conv block
# baseline (speedup 1.0000x reference)
.LBB0_401:
	s_or_b64 exec, exec, s[38:39]
	v_mul_f32_e64 v32, v29, -v35
	ds_bpermute_b32 v33, v96, v32
	v_or_b32_e32 v125, s42, v69
	v_cmp_eq_u32_e32 vcc, 0, v125
	s_and_b32 s43, s54, 7
	s_lshl_b32 s38, s43, 9
	s_waitcnt lgkmcnt(0)
	v_fma_f32 v33, v29, -v35, v33
	v_cndmask_b32_e64 v32, v33, v32, s[0:1]
	ds_bpermute_b32 v33, v97, v32
	s_waitcnt vmcnt(26)
	v_cndmask_b32_e64 v20, v20, 0, vcc
	s_waitcnt vmcnt(25)
	v_cndmask_b32_e64 v126, v30, 0, vcc
	s_waitcnt vmcnt(24)
	v_cndmask_b32_e64 v134, v31, 0, vcc
	v_lshlrev_b32_e32 v30, 16, v20
	s_waitcnt lgkmcnt(0)
	v_add_f32_e32 v33, v32, v33
	v_cndmask_b32_e64 v32, v33, v32, s[14:15]
	ds_bpermute_b32 v33, v98, v32
	v_and_b32_e32 v31, 0xffff0000, v20
	s_waitcnt vmcnt(0)
	v_fma_f32 v128, v4, v30, v6
	v_or_b32_e32 v35, s38, v1
	v_readlane_b32 s60, v253, 18
	s_waitcnt lgkmcnt(0)
	v_add_f32_e32 v33, v32, v33
	v_cndmask_b32_e64 v32, v33, v32, s[4:5]
	ds_bpermute_b32 v33, v99, v32
	v_readlane_b32 s70, v253, 28
	v_readlane_b32 s71, v253, 29
	v_fma_f32 v135, v5, v31, v7
	v_lshlrev_b32_e32 v125, 16, v126
	s_waitcnt lgkmcnt(0)
	v_add_f32_e32 v20, v32, v33
	v_cndmask_b32_e64 v32, v20, v32, s[6:7]
	ds_bpermute_b32 v33, v100, v32
	v_lshlrev_b32_e32 v20, 2, v35
	v_lshlrev_b32_e32 v130, 16, v122
	v_lshlrev_b32_e32 v131, 16, v134
	v_fmac_f32_e32 v128, v8, v125
	s_waitcnt lgkmcnt(0)
	v_add_f32_e32 v30, v32, v33
	v_cndmask_b32_e64 v127, v30, v32, s[8:9]
	ds_bpermute_b32 v129, v101, v127
	v_lshl_add_u64 v[30:31], s[30:31], 0, v[20:21]
	v_lshl_add_u64 v[32:33], s[70:71], 0, v[20:21]
	v_lshlrev_b32_e32 v20, 1, v35
	v_and_b32_e32 v122, 0xffff0000, v122
	s_waitcnt lgkmcnt(0)
	v_add_f32_e32 v35, v127, v129
	v_cndmask_b32_e64 v35, v35, v127, s[10:11]
	v_add_f32_e32 v34, v35, v34
	ds_write2st64_b32 v84, v29, v34 offset0:1 offset1:17
	v_mov_b32_e32 v34, v36
	v_mov_b32_e32 v35, v2
	v_pk_mul_f32 v[132:133], v[34:35], v[130:131]
	v_and_b32_e32 v127, 0xffff0000, v126
	v_add_f32_e32 v2, v133, v128
	v_add_f32_e32 v29, v132, v2
	v_mul_f32_e32 v2, 0xbfb8aa3b, v29
	v_exp_f32_e32 v2, v2
	v_lshlrev_b32_e32 v129, 16, v123
	v_lshlrev_b32_e32 v128, 16, v124
	v_and_b32_e32 v133, 0xffff0000, v123
	v_add_f32_e32 v2, 1.0, v2
	v_and_b32_e32 v132, 0xffff0000, v124
	v_rcp_f32_e32 v124, v2
	v_and_b32_e32 v123, 0xffff0000, v134
	v_mov_b32_e32 v2, v37
	v_fmac_f32_e32 v135, v9, v127
	v_pk_mul_f32 v[36:37], v[2:3], v[122:123]
	v_mul_f32_e32 v29, v29, v124
	v_add_f32_e32 v37, v37, v135
	v_add_f32_e32 v126, v36, v37
	v_mul_f32_e32 v36, 0xbfb8aa3b, v126
	v_exp_f32_e32 v134, v36
	v_mov_b32_e32 v37, v4
	v_mov_b32_e32 v36, v8
	v_mov_b32_e32 v124, v131
	v_add_f32_e32 v4, 1.0, v134
	v_rcp_f32_e32 v4, v4
	v_pk_mul_f32 v[124:125], v[36:37], v[124:125]
	v_pk_mul_f32 v[134:135], v[36:37], v[130:131]
	v_add_f32_e32 v125, v125, v6
	v_mul_f32_e32 v138, v126, v4
	v_mov_b32_e32 v4, v9
	v_mov_b32_e32 v126, v123
	v_pk_mul_f32 v[8:9], v[4:5], v[126:127]
	v_pk_mov_b32 v[126:127], v[128:129], v[130:131] op_sel:[1,0]
	v_add_f32_e32 v124, v124, v125
	v_pk_mul_f32 v[130:131], v[34:35], v[126:127]
	v_add_f32_e32 v135, v135, v6
	v_add_f32_e32 v124, v131, v124
	v_add_f32_e32 v139, v130, v124
	v_mul_f32_e32 v124, 0xbfb8aa3b, v139
	v_exp_f32_e32 v136, v124
	v_add_f32_e32 v134, v134, v135
	v_lshlrev_b32_e32 v131, 16, v120
	v_and_b32_e32 v135, 0xffff0000, v120
	v_add_f32_e32 v136, 1.0, v136
	v_rcp_f32_e32 v140, v136
	v_pk_mul_f32 v[136:137], v[34:35], v[128:129]
	v_lshlrev_b32_e32 v130, 16, v121
	v_add_f32_e32 v134, v137, v134
	v_add_f32_e32 v136, v136, v134
	v_mul_f32_e32 v134, 0xbfb8aa3b, v136
	v_exp_f32_e32 v137, v134
	v_and_b32_e32 v134, 0xffff0000, v121
	v_add_f32_e32 v9, v9, v7
	v_pk_mul_f32 v[124:125], v[4:5], v[122:123]
	v_add_f32_e32 v120, 1.0, v137
	v_rcp_f32_e32 v137, v120
	v_pk_mov_b32 v[120:121], v[132:133], v[122:123] op_sel:[1,0]
	v_add_f32_e32 v8, v8, v9
	v_pk_mul_f32 v[122:123], v[2:3], v[120:121]
	v_mul_f32_e32 v139, v139, v140
	v_add_f32_e32 v8, v123, v8
	v_add_f32_e32 v140, v122, v8
	v_mul_f32_e32 v8, 0xbfb8aa3b, v140
	v_add_f32_e32 v123, v125, v7
	v_exp_f32_e32 v122, v8
	v_pk_mul_f32 v[8:9], v[2:3], v[132:133]
	v_add_f32_e32 v123, v124, v123
	v_add_f32_e32 v9, v9, v123
	v_add_f32_e32 v124, v8, v9
	v_mul_f32_e32 v8, 0xbfb8aa3b, v124
	v_exp_f32_e32 v8, v8
	v_add_f32_e32 v9, 1.0, v122
	v_mul_f32_e32 v136, v136, v137
	v_rcp_f32_e32 v125, v9
	v_add_f32_e32 v8, 1.0, v8
	v_rcp_f32_e32 v137, v8
	v_pk_mul_f32 v[8:9], v[36:37], v[126:127]
	v_mul_f32_e32 v140, v140, v125
	v_add_f32_e32 v9, v9, v6
	v_mul_f32_e32 v137, v124, v137
	v_pk_mov_b32 v[124:125], v[130:131], v[128:129] op_sel:[1,0]
	v_add_f32_e32 v8, v8, v9
	v_pk_mul_f32 v[126:127], v[34:35], v[124:125]
	v_pk_mul_f32 v[122:123], v[36:37], v[128:129]
	v_add_f32_e32 v8, v127, v8
	v_add_f32_e32 v141, v126, v8
	v_mul_f32_e32 v8, 0xbfb8aa3b, v141
	v_exp_f32_e32 v128, v8
	v_add_f32_e32 v123, v123, v6
	v_add_f32_e32 v122, v122, v123
	v_pk_mul_f32 v[120:121], v[4:5], v[120:121]
	v_add_f32_e32 v128, 1.0, v128
	v_rcp_f32_e32 v142, v128
	v_pk_mul_f32 v[128:129], v[34:35], v[130:131]
	v_lshlrev_b32_e32 v127, 16, v118
	v_add_f32_e32 v122, v129, v122
	v_add_f32_e32 v143, v128, v122
	v_mul_f32_e32 v122, 0xbfb8aa3b, v143
	v_exp_f32_e32 v128, v122
	v_and_b32_e32 v123, 0xffff0000, v118
	v_lshlrev_b32_e32 v126, 16, v119
	v_and_b32_e32 v122, 0xffff0000, v119
	v_add_f32_e32 v118, 1.0, v128
	v_mul_f32_e32 v141, v141, v142
	v_rcp_f32_e32 v142, v118
	v_pk_mov_b32 v[118:119], v[134:135], v[132:133] op_sel:[1,0]
	v_add_f32_e32 v121, v121, v7
	v_pk_mul_f32 v[128:129], v[2:3], v[118:119]
	v_add_f32_e32 v120, v120, v121
	v_add_f32_e32 v120, v129, v120
	v_pk_mul_f32 v[8:9], v[4:5], v[132:133]
	v_add_f32_e32 v132, v128, v120
	v_mul_f32_e32 v120, 0xbfb8aa3b, v132
	v_exp_f32_e32 v128, v120
	v_add_f32_e32 v9, v9, v7
	v_add_f32_e32 v8, v8, v9
	v_mul_f32_e32 v142, v143, v142
	v_add_f32_e32 v128, 1.0, v128
	v_rcp_f32_e32 v133, v128
	v_pk_mul_f32 v[128:129], v[2:3], v[134:135]
	v_pk_mul_f32 v[120:121], v[36:37], v[124:125]
	v_add_f32_e32 v8, v129, v8
	v_add_f32_e32 v143, v128, v8
	v_mul_f32_e32 v8, 0xbfb8aa3b, v143
	v_exp_f32_e32 v144, v8
	v_pk_mov_b32 v[8:9], v[126:127], v[130:131] op_sel:[1,0]
	v_add_f32_e32 v121, v121, v6
	v_pk_mul_f32 v[128:129], v[34:35], v[8:9]
	v_add_f32_e32 v120, v120, v121
	v_add_f32_e32 v120, v129, v120
	v_add_f32_e32 v128, v128, v120
	v_mul_f32_e32 v120, 0xbfb8aa3b, v128
	v_exp_f32_e32 v120, v120
	v_pk_mul_f32 v[118:119], v[4:5], v[118:119]
	v_pk_mul_f32 v[124:125], v[36:37], v[130:131]
	v_pk_mov_b32 v[130:131], v[122:123], v[134:135] op_sel:[1,0]
	v_add_f32_e32 v120, 1.0, v120
	v_rcp_f32_e32 v129, v120
	v_add_f32_e32 v119, v119, v7
	v_add_f32_e32 v121, 1.0, v144
	v_mul_f32_e32 v144, v132, v133
	v_pk_mul_f32 v[132:133], v[2:3], v[130:131]
	v_add_f32_e32 v118, v118, v119
	v_add_f32_e32 v118, v133, v118
	v_mul_f32_e32 v145, v128, v129
	v_pk_mul_f32 v[128:129], v[34:35], v[126:127]
	v_add_f32_e32 v127, v132, v118
	v_rcp_f32_e32 v121, v121
	v_mul_f32_e32 v118, 0xbfb8aa3b, v127
	v_exp_f32_e32 v118, v118
	v_add_f32_e32 v125, v125, v6
	v_mul_f32_e32 v143, v143, v121
	v_pk_mul_f32 v[120:121], v[4:5], v[134:135]
	v_add_f32_e32 v119, v124, v125
	v_add_f32_e32 v119, v129, v119
	v_add_f32_e32 v118, 1.0, v118
	v_add_f32_e32 v121, v121, v7
	v_add_f32_e32 v124, v128, v119
	v_rcp_f32_e32 v125, v118
	v_pk_mul_f32 v[118:119], v[2:3], v[122:123]
	v_add_f32_e32 v120, v120, v121
	v_add_f32_e32 v119, v119, v120
	v_add_f32_e32 v123, v118, v119
	v_mul_f32_e32 v118, 0xbfb8aa3b, v124
	v_exp_f32_e32 v118, v118
	v_mul_f32_e32 v119, 0xbfb8aa3b, v123
	v_exp_f32_e32 v119, v119
	v_pk_mul_f32 v[8:9], v[36:37], v[8:9]
	v_lshlrev_b32_e32 v120, 16, v117
	v_mov_b32_e32 v121, v126
	v_add_f32_e32 v9, v9, v6
	v_add_f32_e32 v118, 1.0, v118
	v_pk_mul_f32 v[120:121], v[34:35], v[120:121]
	v_add_f32_e32 v8, v8, v9
	v_mul_f32_e32 v125, v127, v125
	v_rcp_f32_e32 v127, v118
	v_add_f32_e32 v128, 1.0, v119
	v_pk_mul_f32 v[118:119], v[4:5], v[130:131]
	v_add_f32_e32 v8, v121, v8
	v_add_f32_e32 v120, v120, v8
	v_and_b32_e32 v8, 0xffff0000, v117
	v_mov_b32_e32 v9, v122
	v_add_f32_e32 v117, v119, v7
	v_pk_mul_f32 v[8:9], v[2:3], v[8:9]
	v_add_f32_e32 v117, v118, v117
	v_add_f32_e32 v9, v9, v117
	v_add_f32_e32 v8, v8, v9
	v_mul_f32_e32 v9, 0xbfb8aa3b, v120
	v_mul_f32_e32 v117, 0xbfb8aa3b, v8
	v_exp_f32_e32 v9, v9
	v_exp_f32_e32 v117, v117
	v_rcp_f32_e32 v118, v128
	v_mul_f32_e32 v121, v124, v127
	v_add_f32_e32 v9, 1.0, v9
	v_add_f32_e32 v117, 1.0, v117
	v_rcp_f32_e32 v9, v9
	v_rcp_f32_e32 v117, v117
	v_mul_f32_e32 v126, v123, v118
	v_cvt_pk_bf16_f32 v118, v29, v139
	v_mul_f32_e32 v9, v120, v9
	v_mul_f32_e32 v8, v8, v117
	v_cvt_pk_bf16_f32 v119, v136, v141
	v_cvt_pk_bf16_f32 v120, v142, v145
	v_cvt_pk_bf16_f32 v121, v121, v9
	v_cvt_pk_bf16_f32 v122, v138, v140
	v_cvt_pk_bf16_f32 v123, v137, v144
	v_cvt_pk_bf16_f32 v124, v143, v125
	v_cvt_pk_bf16_f32 v125, v126, v8
	v_lshlrev_b32_e32 v8, 16, v116
	v_lshlrev_b32_e32 v9, 16, v113
	ds_write_b128 v85, v[118:121] offset:8192
	ds_write_b128 v85, v[122:125] offset:8464
	v_pk_mul_f32 v[118:119], v[36:37], v[8:9]
	v_lshlrev_b32_e32 v123, 16, v114
	v_lshlrev_b32_e32 v122, 16, v57
	v_add_f32_e32 v9, v119, v6
	v_pk_mul_f32 v[126:127], v[34:35], v[122:123]
	v_add_f32_e32 v9, v118, v9
	v_add_f32_e32 v9, v127, v9
	v_and_b32_e32 v117, 0xffff0000, v113
	v_and_b32_e32 v116, 0xffff0000, v116
	v_add_f32_e32 v9, v126, v9
	v_pk_mul_f32 v[120:121], v[4:5], v[116:117]
	v_mul_f32_e32 v29, 0xbfb8aa3b, v9
	v_and_b32_e32 v125, 0xffff0000, v114
	v_exp_f32_e32 v29, v29
	v_and_b32_e32 v124, 0xffff0000, v57
	v_add_f32_e32 v57, v121, v7
	v_pk_mul_f32 v[126:127], v[2:3], v[124:125]
	v_add_f32_e32 v57, v120, v57
	v_add_f32_e32 v57, v127, v57
	v_add_f32_e32 v57, v126, v57
	v_add_f32_e32 v29, 1.0, v29
	v_mul_f32_e32 v113, 0xbfb8aa3b, v57
	v_rcp_f32_e32 v29, v29
	v_exp_f32_e32 v114, v113
	v_lshlrev_b32_e32 v119, 16, v112
	v_lshlrev_b32_e32 v118, 16, v115
	v_mul_f32_e32 v29, v9, v29
	v_add_f32_e32 v9, 1.0, v114
	v_rcp_f32_e32 v120, v9
	v_pk_mov_b32 v[8:9], v[122:123], v[8:9] op_sel:[1,0]
	v_and_b32_e32 v113, 0xffff0000, v112
	v_pk_mul_f32 v[8:9], v[36:37], v[8:9]
	v_mul_f32_e32 v128, v57, v120
	v_pk_mov_b32 v[120:121], v[118:119], v[122:123] op_sel:[1,0]
	v_add_f32_e32 v9, v9, v6
	v_and_b32_e32 v112, 0xffff0000, v115
	v_pk_mul_f32 v[114:115], v[36:37], v[122:123]
	v_pk_mul_f32 v[122:123], v[34:35], v[120:121]
	v_add_f32_e32 v8, v8, v9
	v_add_f32_e32 v8, v123, v8
	v_add_f32_e32 v129, v122, v8
	v_mul_f32_e32 v8, 0xbfb8aa3b, v129
	v_exp_f32_e32 v57, v8
	v_pk_mul_f32 v[126:127], v[34:35], v[118:119]
	v_pk_mov_b32 v[116:117], v[124:125], v[116:117] op_sel:[1,0]
	v_lshlrev_b32_e32 v123, 16, v55
	v_add_f32_e32 v57, 1.0, v57
	v_rcp_f32_e32 v130, v57
	v_add_f32_e32 v57, v115, v6
	v_add_f32_e32 v57, v114, v57
	v_add_f32_e32 v57, v127, v57
	v_add_f32_e32 v126, v126, v57
	v_mul_f32_e32 v57, 0xbfb8aa3b, v126
	v_exp_f32_e32 v114, v57
	v_pk_mul_f32 v[116:117], v[4:5], v[116:117]
	v_and_b32_e32 v57, 0xffff0000, v55
	v_add_f32_e32 v117, v117, v7
	v_add_f32_e32 v55, 1.0, v114
	v_pk_mov_b32 v[114:115], v[112:113], v[124:125] op_sel:[1,0]
	v_pk_mul_f32 v[8:9], v[4:5], v[124:125]
	v_pk_mul_f32 v[124:125], v[2:3], v[114:115]
	v_add_f32_e32 v116, v116, v117
	v_add_f32_e32 v116, v125, v116
	v_add_f32_e32 v124, v124, v116
	v_mul_f32_e32 v116, 0xbfb8aa3b, v124
	v_add_f32_e32 v9, v9, v7
	v_exp_f32_e32 v125, v116
	v_pk_mul_f32 v[116:117], v[2:3], v[112:113]
	v_add_f32_e32 v8, v8, v9
	v_add_f32_e32 v8, v117, v8
	v_mul_f32_e32 v127, v129, v130
	v_add_f32_e32 v129, v116, v8
	v_mul_f32_e32 v8, 0xbfb8aa3b, v129
	v_exp_f32_e32 v8, v8
	v_rcp_f32_e32 v55, v55
	v_add_f32_e32 v9, 1.0, v125
	v_lshlrev_b32_e32 v122, 16, v56
	v_add_f32_e32 v8, 1.0, v8
	v_mul_f32_e32 v126, v126, v55
	v_rcp_f32_e32 v55, v9
	v_rcp_f32_e32 v125, v8
	v_pk_mul_f32 v[8:9], v[36:37], v[120:121]
	v_pk_mul_f32 v[116:117], v[36:37], v[118:119]
	v_pk_mov_b32 v[118:119], v[122:123], v[118:119] op_sel:[1,0]
	v_add_f32_e32 v9, v9, v6
	v_pk_mul_f32 v[120:121], v[34:35], v[118:119]
	v_add_f32_e32 v8, v8, v9
	v_add_f32_e32 v8, v121, v8
	v_add_f32_e32 v131, v120, v8
	v_mul_f32_e32 v8, 0xbfb8aa3b, v131
	v_mul_f32_e32 v130, v124, v55
	v_exp_f32_e32 v55, v8
	v_mul_f32_e32 v129, v129, v125
	v_pk_mul_f32 v[124:125], v[34:35], v[122:123]
	v_and_b32_e32 v56, 0xffff0000, v56
	v_add_f32_e32 v55, 1.0, v55
	v_rcp_f32_e32 v132, v55
	v_add_f32_e32 v55, v117, v6
	v_add_f32_e32 v55, v116, v55
	v_add_f32_e32 v55, v125, v55
	v_add_f32_e32 v124, v124, v55
	v_mul_f32_e32 v55, 0xbfb8aa3b, v124
	v_exp_f32_e32 v116, v55
	v_pk_mul_f32 v[114:115], v[4:5], v[114:115]
	v_pk_mul_f32 v[8:9], v[4:5], v[112:113]
	v_pk_mov_b32 v[112:113], v[56:57], v[112:113] op_sel:[1,0]
	v_add_f32_e32 v116, 1.0, v116
	v_add_f32_e32 v115, v115, v7
	v_rcp_f32_e32 v125, v116
	v_pk_mul_f32 v[116:117], v[2:3], v[112:113]
	v_add_f32_e32 v114, v114, v115
	v_add_f32_e32 v114, v117, v114
	v_lshlrev_b32_e32 v121, 16, v53
	v_and_b32_e32 v55, 0xffff0000, v53
	v_mul_f32_e32 v53, v131, v132
	v_add_f32_e32 v131, v116, v114
	v_mul_f32_e32 v114, 0xbfb8aa3b, v131
	v_exp_f32_e32 v132, v114
	v_pk_mul_f32 v[114:115], v[36:37], v[118:119]
	v_add_f32_e32 v9, v9, v7
	v_mul_f32_e32 v124, v124, v125
	v_add_f32_e32 v118, 1.0, v132
	v_rcp_f32_e32 v125, v118
	v_pk_mul_f32 v[118:119], v[2:3], v[56:57]
	v_add_f32_e32 v8, v8, v9
	v_add_f32_e32 v8, v119, v8
	v_add_f32_e32 v132, v118, v8
	v_lshlrev_b32_e32 v120, 16, v54
	v_mul_f32_e32 v8, 0xbfb8aa3b, v132
	v_exp_f32_e32 v133, v8
	v_pk_mov_b32 v[8:9], v[120:121], v[122:123] op_sel:[1,0]
	v_add_f32_e32 v115, v115, v6
	v_pk_mul_f32 v[118:119], v[34:35], v[8:9]
	v_add_f32_e32 v114, v114, v115
	v_add_f32_e32 v114, v119, v114
	v_add_f32_e32 v118, v118, v114
	v_mul_f32_e32 v114, 0xbfb8aa3b, v118
	v_exp_f32_e32 v114, v114
	v_add_f32_e32 v115, 1.0, v133
	v_rcp_f32_e32 v115, v115
	v_and_b32_e32 v54, 0xffff0000, v54
	v_add_f32_e32 v114, 1.0, v114
	v_rcp_f32_e32 v119, v114
	v_pk_mul_f32 v[112:113], v[4:5], v[112:113]
	v_mul_f32_e32 v125, v131, v125
	v_mul_f32_e32 v131, v132, v115
	v_pk_mul_f32 v[114:115], v[4:5], v[56:57]
	v_pk_mov_b32 v[56:57], v[54:55], v[56:57] op_sel:[1,0]
	v_add_f32_e32 v113, v113, v7
	v_pk_mul_f32 v[116:117], v[36:37], v[122:123]
	v_pk_mul_f32 v[122:123], v[2:3], v[56:57]
	v_add_f32_e32 v112, v112, v113
	v_add_f32_e32 v112, v123, v112
	v_mul_f32_e32 v132, v118, v119
	v_pk_mul_f32 v[118:119], v[34:35], v[120:121]
	v_add_f32_e32 v121, v122, v112
	v_mul_f32_e32 v112, 0xbfb8aa3b, v121
	v_exp_f32_e32 v112, v112
	v_add_f32_e32 v117, v117, v6
	v_add_f32_e32 v113, v116, v117
	v_add_f32_e32 v113, v119, v113
	v_add_f32_e32 v112, 1.0, v112
	v_pk_mul_f32 v[8:9], v[36:37], v[8:9]
	v_add_f32_e32 v116, v118, v113
	v_rcp_f32_e32 v117, v112
	v_pk_mul_f32 v[112:113], v[2:3], v[54:55]
	v_add_f32_e32 v55, v115, v7
	v_pk_mul_f32 v[4:5], v[4:5], v[56:57]
	v_lshlrev_b32_e32 v36, 16, v52
	v_mov_b32_e32 v37, v120
	v_add_f32_e32 v6, v9, v6
	v_add_f32_e32 v55, v114, v55
	v_pk_mul_f32 v[34:35], v[34:35], v[36:37]
	v_add_f32_e32 v6, v8, v6
	v_and_b32_e32 v8, 0xffff0000, v52
	v_mov_b32_e32 v9, v54
	v_add_f32_e32 v5, v5, v7
	v_add_f32_e32 v55, v113, v55
	v_add_f32_e32 v6, v35, v6
	v_pk_mul_f32 v[2:3], v[2:3], v[8:9]
	v_add_f32_e32 v4, v4, v5
	v_add_f32_e32 v55, v112, v55
	v_add_f32_e32 v6, v34, v6
	v_add_f32_e32 v3, v3, v4
	v_mul_f32_e32 v112, 0xbfb8aa3b, v116
	v_mul_f32_e32 v113, 0xbfb8aa3b, v55
	v_add_f32_e32 v2, v2, v3
	v_mul_f32_e32 v3, 0xbfb8aa3b, v6
	v_exp_f32_e32 v112, v112
	v_exp_f32_e32 v113, v113
	v_exp_f32_e32 v3, v3
	v_mul_f32_e32 v4, 0xbfb8aa3b, v2
	v_exp_f32_e32 v4, v4
	v_add_f32_e32 v112, 1.0, v112
	v_add_f32_e32 v113, 1.0, v113
	v_add_f32_e32 v3, 1.0, v3
	v_rcp_f32_e32 v112, v112
	v_rcp_f32_e32 v5, v113
	v_rcp_f32_e32 v3, v3
	v_add_f32_e32 v4, 1.0, v4
	v_rcp_f32_e32 v4, v4
	v_mul_f32_e32 v7, v116, v112
	v_mul_f32_e32 v9, v55, v5
	v_mul_f32_e32 v5, v6, v3
	v_mul_f32_e32 v114, v121, v117
	v_mul_f32_e32 v34, v2, v4
	v_cvt_pk_bf16_f32 v2, v29, v127
	v_cvt_pk_bf16_f32 v3, v126, v53
	v_cvt_pk_bf16_f32 v4, v124, v132
	v_cvt_pk_bf16_f32 v5, v7, v5
	v_cvt_pk_bf16_f32 v6, v128, v130
	v_cvt_pk_bf16_f32 v7, v129, v125
	v_cvt_pk_bf16_f32 v8, v131, v114
	v_cvt_pk_bf16_f32 v9, v9, v34
	ds_write_b128 v85, v[2:5] offset:8320
	ds_write_b128 v85, v[6:9] offset:8592
	s_waitcnt lgkmcnt(0)
	s_barrier
	v_cndmask_b32_e64 v3, v50, 0, s[12:13]
	v_cndmask_b32_e64 v9, v51, 0, s[12:13]
	ds_read_b32 v29, v21 offset:4604
	ds_read_b128 v[50:53], v86 offset:4096
	v_cndmask_b32_e64 v2, v49, 0, s[12:13]
	v_lshlrev_b32_e32 v4, 16, v2
	v_fma_f32 v36, v12, v4, v14
	v_lshlrev_b32_e32 v37, 16, v3
	s_waitcnt lgkmcnt(0)
	v_sub_f32_e32 v34, v29, v50
	v_mul_f32_e32 v34, 0x3fb8aa3b, v34
	v_exp_f32_e32 v113, v34
	v_lshlrev_b32_e32 v117, 16, v9
	v_lshlrev_b32_e32 v116, 16, v45
	v_mov_b32_e32 v34, v18
	v_mov_b32_e32 v35, v10
	v_fmac_f32_e32 v36, v16, v37
	v_pk_mul_f32 v[118:119], v[34:35], v[116:117]
	v_and_b32_e32 v2, 0xffff0000, v2
	v_add_f32_e32 v10, v119, v36
	v_add_f32_e32 v10, v118, v10
	v_mul_f32_e32 v18, 0xbfb8aa3b, v10
	v_exp_f32_e32 v18, v18
	v_fma_f32 v57, v13, v2, v15
	v_and_b32_e32 v49, 0xffff0000, v3
	v_lshlrev_b32_e32 v115, 16, v46
	v_add_f32_e32 v18, 1.0, v18
	v_rcp_f32_e32 v18, v18
	v_and_b32_e32 v119, 0xffff0000, v46
	v_and_b32_e32 v121, 0xffff0000, v9
	v_and_b32_e32 v120, 0xffff0000, v45
	v_mul_f32_e32 v46, v10, v18
	v_mov_b32_e32 v10, v19
	v_fmac_f32_e32 v57, v17, v49
	v_pk_mul_f32 v[18:19], v[10:11], v[120:121]
	ds_read_b128 v[2:5], v86
	ds_read_b96 v[6:8], v86 offset:16
	ds_read_b96 v[54:56], v86 offset:4112
	v_add_f32_e32 v9, v19, v57
	v_add_f32_e32 v18, v18, v9
	v_mul_f32_e32 v9, 0xbfb8aa3b, v18
	v_exp_f32_e32 v9, v9
	v_sub_f32_e32 v36, v29, v51
	v_lshlrev_b32_e32 v114, 16, v48
	v_and_b32_e32 v118, 0xffff0000, v48
	v_add_f32_e32 v9, 1.0, v9
	v_rcp_f32_e32 v112, v9
	v_mul_f32_e32 v36, 0x3fb8aa3b, v36
	v_mov_b32_e32 v123, v12
	s_waitcnt lgkmcnt(2)
	v_mov_b32_e32 v19, v2
	v_mov_b32_e32 v12, v17
	v_mov_b32_e32 v48, v121
	v_fma_f32 v2, v13, v49, v15
	v_exp_f32_e32 v51, v36
	v_mov_b32_e32 v122, v16
	v_mov_b32_e32 v36, v117
	v_pk_mul_f32 v[18:19], v[18:19], v[112:113]
	v_pk_fma_f32 v[16:17], v[12:13], v[48:49], v[2:3] op_sel_hi:[1,1,0]
	v_fma_f32 v2, v13, v121, v15
	v_pk_mul_f32 v[36:37], v[122:123], v[36:37]
	v_mul_f32_e32 v57, v46, v19
	v_mul_f32_e32 v126, v18, v19
	v_pk_fma_f32 v[18:19], v[12:13], v[120:121], v[2:3] op_sel_hi:[1,1,0]
	v_sub_f32_e32 v2, v29, v52
	v_mul_f32_e32 v2, 0x3fb8aa3b, v2
	v_lshlrev_b32_e32 v48, 16, v47
	v_and_b32_e32 v112, 0xffff0000, v47
	v_pk_mov_b32 v[46:47], v[114:115], v[116:117] op_sel:[1,0]
	v_add_f32_e32 v9, v37, v14
	v_exp_f32_e32 v45, v2
	v_sub_f32_e32 v2, v29, v53
	v_pk_mul_f32 v[52:53], v[34:35], v[46:47]
	v_add_f32_e32 v9, v36, v9
	v_add_f32_e32 v9, v53, v9
	v_pk_mul_f32 v[124:125], v[122:123], v[116:117]
	v_add_f32_e32 v9, v52, v9
	v_mul_f32_e32 v36, 0xbfb8aa3b, v9
	v_add_f32_e32 v50, v125, v14
	v_lshlrev_b32_e32 v49, 16, v44
	v_and_b32_e32 v113, 0xffff0000, v44
	v_exp_f32_e32 v44, v36
	v_pk_mul_f32 v[36:37], v[34:35], v[114:115]
	v_add_f32_e32 v50, v124, v50
	v_add_f32_e32 v37, v37, v50
	v_add_f32_e32 v36, v36, v37
	v_mul_f32_e32 v37, 0xbfb8aa3b, v36
	v_exp_f32_e32 v50, v37
	v_mul_f32_e32 v2, 0x3fb8aa3b, v2
	v_exp_f32_e32 v37, v2
	v_add_f32_e32 v2, 1.0, v44
	v_rcp_f32_e32 v44, v2
	v_add_f32_e32 v2, 1.0, v50
	v_pk_mov_b32 v[52:53], v[118:119], v[120:121] op_sel:[1,0]
	v_rcp_f32_e32 v50, v2
	v_mul_f32_e32 v2, v11, v53
	v_pk_add_f32 v[16:17], v[2:3], v[16:17] op_sel_hi:[0,1]
	v_pk_fma_f32 v[16:17], v[10:11], v[52:53], v[16:17]
	v_mul_f32_e32 v36, v36, v50
	v_mul_f32_e32 v2, 0xbfb8aa3b, v16
	v_exp_f32_e32 v2, v2
	v_mov_b32_e32 v17, v3
	v_mul_f32_e32 v9, v9, v44
	v_pk_mul_f32 v[46:47], v[122:123], v[46:47]
	v_add_f32_e32 v2, 1.0, v2
	v_rcp_f32_e32 v50, v2
	v_mul_f32_e32 v2, v11, v119
	v_pk_add_f32 v[18:19], v[2:3], v[18:19] op_sel_hi:[0,1]
	v_pk_fma_f32 v[18:19], v[10:11], v[118:119], v[18:19]
	v_pk_mul_f32 v[116:117], v[122:123], v[114:115]
	v_mul_f32_e32 v2, 0xbfb8aa3b, v18
	v_exp_f32_e32 v19, v2
	v_pk_mul_f32 v[2:3], v[16:17], v[50:51]
	v_and_b32_e32 v51, 0xffff0000, v41
	v_mul_f32_e32 v120, v9, v3
	v_add_f32_e32 v16, 1.0, v19
	v_rcp_f32_e32 v44, v16
	v_mov_b32_e32 v19, v4
	v_mul_f32_e32 v121, v2, v3
	v_fma_f32 v4, v13, v119, v15
	v_pk_mul_f32 v[2:3], v[18:19], v[44:45]
	v_pk_fma_f32 v[16:17], v[12:13], v[118:119], v[4:5] op_sel_hi:[1,1,0]
	v_mul_f32_e32 v125, v2, v3
	v_fma_f32 v2, v13, v53, v15
	s_waitcnt lgkmcnt(0)
	v_sub_f32_e32 v4, v29, v54
	v_mul_f32_e32 v124, v36, v3
	v_pk_fma_f32 v[2:3], v[12:13], v[52:53], v[2:3] op_sel_hi:[1,1,0]
	v_mul_f32_e32 v4, 0x3fb8aa3b, v4
	v_pk_mov_b32 v[52:53], v[48:49], v[114:115] op_sel:[1,0]
	v_add_f32_e32 v9, v47, v14
	v_exp_f32_e32 v19, v4
	v_sub_f32_e32 v4, v29, v55
	v_pk_mul_f32 v[54:55], v[34:35], v[52:53]
	v_add_f32_e32 v9, v46, v9
	v_add_f32_e32 v36, v117, v14
	v_add_f32_e32 v9, v55, v9
	v_pk_mul_f32 v[46:47], v[34:35], v[48:49]
	v_add_f32_e32 v36, v116, v36
	v_add_f32_e32 v9, v54, v9
	v_add_f32_e32 v36, v47, v36
	v_mul_f32_e32 v18, 0xbfb8aa3b, v9
	v_add_f32_e32 v36, v46, v36
	v_lshlrev_b32_e32 v45, 16, v41
	v_exp_f32_e32 v18, v18
	v_mul_f32_e32 v41, 0xbfb8aa3b, v36
	v_exp_f32_e32 v41, v41
	v_mul_f32_e32 v4, 0x3fb8aa3b, v4
	v_exp_f32_e32 v47, v4
	v_add_f32_e32 v4, 1.0, v18
	v_rcp_f32_e32 v18, v4
	v_add_f32_e32 v4, 1.0, v41
	v_pk_mov_b32 v[54:55], v[112:113], v[118:119] op_sel:[1,0]
	v_rcp_f32_e32 v41, v4
	v_mul_f32_e32 v4, v11, v55
	v_pk_add_f32 v[2:3], v[4:5], v[2:3] op_sel_hi:[0,1]
	v_pk_fma_f32 v[2:3], v[10:11], v[54:55], v[2:3]
	v_mul_f32_e32 v4, v11, v113
	v_mul_f32_e32 v3, 0xbfb8aa3b, v2
	v_exp_f32_e32 v3, v3
	v_pk_add_f32 v[16:17], v[4:5], v[16:17] op_sel_hi:[0,1]
	v_pk_fma_f32 v[16:17], v[10:11], v[112:113], v[16:17]
	v_mul_f32_e32 v41, v36, v41
	v_add_f32_e32 v3, 1.0, v3
	v_rcp_f32_e32 v36, v3
	v_mul_f32_e32 v3, 0xbfb8aa3b, v16
	v_exp_f32_e32 v4, v3
	v_mul_f32_e32 v9, v9, v18
	v_lshlrev_b32_e32 v44, 16, v43
	v_pk_mul_f32 v[52:53], v[122:123], v[52:53]
	v_add_f32_e32 v4, 1.0, v4
	v_rcp_f32_e32 v18, v4
	v_mov_b32_e32 v3, v5
	v_pk_mul_f32 v[2:3], v[2:3], v[36:37]
	v_mov_b32_e32 v17, v6
	v_pk_mov_b32 v[4:5], v[44:45], v[48:49] op_sel:[1,0]
	v_add_f32_e32 v6, v53, v14
	v_and_b32_e32 v50, 0xffff0000, v43
	v_mul_f32_e32 v43, v9, v3
	v_mul_f32_e32 v116, v2, v3
	v_pk_mul_f32 v[2:3], v[16:17], v[18:19]
	v_pk_mul_f32 v[16:17], v[34:35], v[4:5]
	v_add_f32_e32 v6, v52, v6
	v_add_f32_e32 v6, v17, v6
	v_add_f32_e32 v9, v16, v6
	v_mul_f32_e32 v6, 0xbfb8aa3b, v9
	v_exp_f32_e32 v6, v6
	v_pk_mul_f32 v[114:115], v[122:123], v[48:49]
	v_mul_f32_e32 v41, v41, v3
	v_mul_f32_e32 v48, v2, v3
	v_add_f32_e32 v3, 1.0, v6
	v_rcp_f32_e32 v18, v3
	v_fma_f32 v2, v13, v55, v15
	v_fma_f32 v6, v13, v113, v15
	v_pk_fma_f32 v[2:3], v[12:13], v[54:55], v[2:3] op_sel_hi:[1,1,0]
	v_mul_f32_e32 v9, v9, v18
	v_pk_mov_b32 v[18:19], v[50:51], v[112:113] op_sel:[1,0]
	v_pk_fma_f32 v[16:17], v[12:13], v[112:113], v[6:7] op_sel_hi:[1,1,0]
	v_mul_f32_e32 v6, v11, v19
	v_pk_add_f32 v[2:3], v[6:7], v[2:3] op_sel_hi:[0,1]
	v_pk_fma_f32 v[2:3], v[10:11], v[18:19], v[2:3]
	v_add_f32_e32 v6, v115, v14
	v_mul_f32_e32 v3, 0xbfb8aa3b, v2
	v_exp_f32_e32 v3, v3
	v_pk_mul_f32 v[36:37], v[34:35], v[44:45]
	v_add_f32_e32 v6, v114, v6
	v_pk_mul_f32 v[4:5], v[122:123], v[4:5]
	v_add_f32_e32 v3, 1.0, v3
	v_rcp_f32_e32 v46, v3
	v_add_f32_e32 v3, v37, v6
	v_add_f32_e32 v36, v36, v3
	v_mov_b32_e32 v3, v7
	v_mul_f32_e32 v6, v11, v51
	v_pk_mul_f32 v[2:3], v[2:3], v[46:47]
	v_pk_add_f32 v[6:7], v[6:7], v[16:17] op_sel_hi:[0,1]
	v_mul_f32_e32 v37, v9, v3
	v_pk_fma_f32 v[6:7], v[10:11], v[50:51], v[6:7]
	v_mul_f32_e32 v9, 0xbfb8aa3b, v36
	v_exp_f32_e32 v9, v9
	v_mul_f32_e32 v16, 0xbfb8aa3b, v6
	v_exp_f32_e32 v16, v16
	v_sub_f32_e32 v7, v29, v56
	v_mul_f32_e32 v7, 0x3fb8aa3b, v7
	v_exp_f32_e32 v17, v7
	v_add_f32_e32 v7, 1.0, v9
	v_rcp_f32_e32 v7, v7
	v_add_f32_e32 v9, 1.0, v16
	v_rcp_f32_e32 v16, v9
	v_mul_f32_e32 v45, v2, v3
	v_mul_f32_e32 v9, v36, v7
	v_mov_b32_e32 v7, v8
	v_pk_mul_f32 v[2:3], v[6:7], v[16:17]
	v_lshlrev_b32_e32 v8, 16, v39
	v_mul_f32_e32 v16, v9, v3
	v_mov_b32_e32 v9, v44
	v_add_f32_e32 v5, v5, v14
	v_pk_mul_f32 v[8:9], v[34:35], v[8:9]
	v_add_f32_e32 v4, v4, v5
	v_fma_f32 v6, v13, v19, v15
	v_add_f32_e32 v4, v9, v4
	v_pk_fma_f32 v[6:7], v[12:13], v[18:19], v[6:7] op_sel_hi:[1,1,0]
	v_add_f32_e32 v13, v8, v4
	ds_read2st64_b32 v[8:9], v88 offset1:16
	v_mul_f32_e32 v12, v11, v50
	v_and_b32_e32 v4, 0xffff0000, v39
	v_mov_b32_e32 v5, v50
	v_pk_add_f32 v[6:7], v[12:13], v[6:7] op_sel_hi:[0,1]
	v_pk_fma_f32 v[4:5], v[10:11], v[4:5], v[6:7]
	v_mul_f32_e32 v6, 0xbfb8aa3b, v13
	v_exp_f32_e32 v6, v6
	v_mul_f32_e32 v7, 0xbfb8aa3b, v4
	s_waitcnt lgkmcnt(0)
	v_sub_f32_e32 v5, v29, v9
	v_exp_f32_e32 v9, v7
	v_mul_f32_e32 v5, 0x3fb8aa3b, v5
	s_lshr_b32 s39, s55, 3
	v_exp_f32_e32 v7, v5
	v_add_f32_e32 v5, 1.0, v6
	s_and_b32 s39, s39, 63
	v_rcp_f32_e32 v5, v5
	v_add_f32_e32 v6, 1.0, v9
	s_lshl_b32 s58, s39, 7
	v_rcp_f32_e32 v6, v6
	s_add_i32 s58, s58, s41
	v_add_u32_e32 v18, s58, v67
	v_mul_f32_e32 v10, v13, v5
	v_mov_b32_e32 v5, v8
	s_lshl_b32 s60, s40, 6
	s_lshl_b32 s59, s40, 12
	v_mad_i64_i32 v[18:19], s[40:41], v18, s45, v[20:21]
	v_mul_f32_e32 v9, v2, v3
	v_pk_mul_f32 v[2:3], v[4:5], v[6:7]
	v_lshl_add_u64 v[34:35], v[18:19], 0, s[34:35]
	v_add_u32_e32 v18, s58, v23
	v_mul_f32_e32 v5, v10, v3
	v_mul_f32_e32 v10, v2, v3
	v_cvt_pk_bf16_f32 v2, v57, v120
	v_cvt_pk_bf16_f32 v3, v124, v43
	v_cvt_pk_bf16_f32 v4, v41, v37
	v_mad_i64_i32 v[36:37], s[40:41], v18, s45, v[20:21]
	v_add_u32_e32 v18, s58, v38
	v_mad_i64_i32 v[18:19], s[40:41], v18, s45, v[20:21]
	v_lshl_add_u64 v[38:39], v[18:19], 0, s[34:35]
	v_add_u32_e32 v18, s58, v40
	v_mad_i64_i32 v[18:19], s[40:41], v18, s45, v[20:21]
	v_lshl_add_u64 v[40:41], v[18:19], 0, s[34:35]
	v_add_u32_e32 v18, s58, v42
	s_lshl_b32 s42, s43, 3
	s_lshl_b32 s43, s39, 6
	v_mad_i64_i32 v[18:19], s[40:41], v18, s45, v[20:21]
	s_or_b32 s40, s59, s43
	s_or_b32 s40, s40, s42
	s_ashr_i32 s41, s40, 31
	v_cvt_pk_bf16_f32 v5, v16, v5
	s_lshl_b64 s[40:41], s[40:41], 2
	v_readlane_b32 s61, v253, 19
	v_cvt_pk_bf16_f32 v6, v126, v121
	v_cvt_pk_bf16_f32 v7, v125, v116
	v_cvt_pk_bf16_f32 v8, v48, v45
	v_cvt_pk_bf16_f32 v9, v9, v10
	ds_write_b128 v91, v[2:5] offset:43008
	ds_write_b128 v91, v[6:9] offset:43280
	s_add_u32 s58, s40, 0x66000000
	ds_read_b128 v[14:17], v106 offset:8192
	ds_read_b128 v[10:13], v106 offset:8256
	ds_read_b128 v[6:9], v106 offset:8320
	ds_read_b128 v[2:5], v106 offset:8384
	s_addc_u32 s61, s41, 0
	s_or_b32 s40, s60, s39
	s_ashr_i32 s41, s40, 31
	s_lshl_b64 s[40:41], s[40:41], 12
	v_lshl_add_u64 v[42:43], v[18:19], 0, s[34:35]
	v_or_b32_e32 v18, s40, v22
	v_mov_b32_e32 v19, s41
	v_or_b32_e32 v18, s38, v18
	v_readlane_b32 s62, v253, 20
	v_lshlrev_b64 v[18:19], 8, v[18:19]
	s_mov_b32 s26, 0
	v_lshl_add_u64 v[44:45], v[26:27], 0, v[18:19]
	s_mov_b64 s[38:39], 0
	s_mov_b32 s62, 0
	v_readlane_b32 s63, v253, 21
	v_readlane_b32 s64, v253, 22
	v_readlane_b32 s65, v253, 23
	v_readlane_b32 s66, v253, 24
	v_readlane_b32 s67, v253, 25
	v_readlane_b32 s68, v253, 26
	v_readlane_b32 s69, v253, 27
	v_readlane_b32 s72, v253, 30
	v_readlane_b32 s73, v253, 31
	v_readlane_b32 s74, v253, 32
	v_readlane_b32 s75, v253, 33
	s_mov_b32 s76, 0x45c00000
	s_mov_b32 s77, 0
	s_movk_i32 s78, 0x3000
	s_mov_b32 s79, 0
	s_movk_i32 s80, 0x6000
	s_mov_b32 s81, 0
	v_lshl_add_u64 v[190:191], s[92:93], 0, v[42:43]
	v_lshl_add_u64 v[192:193], s[92:93], 0, v[40:41]
	v_lshl_add_u64 v[194:195], s[92:93], 0, v[38:39]
	v_lshl_add_u64 v[196:197], s[92:93], 0, v[36:37]
	global_load_dword v168, v[190:191], off
	global_load_dword v169, v[192:193], off
	global_load_dword v170, v[194:195], off
	v_lshl_add_u64 v[196:197], v[196:197], 0, s[76:77]
	global_load_dword v171, v[196:197], off offset:128
	v_lshl_add_u64 v[196:197], v[196:197], 0, s[78:79]
	global_load_dword v172, v[196:197], off offset:128
	v_lshl_add_u64 v[196:197], v[196:197], 0, s[78:79]
	global_load_dword v173, v[196:197], off offset:128
	v_lshl_add_u64 v[196:197], v[196:197], 0, s[78:79]
	global_load_dword v174, v[196:197], off offset:128
	v_lshl_add_u64 v[196:197], v[196:197], 0, s[78:79]
	global_load_dword v175, v[196:197], off offset:128
	v_lshl_add_u64 v[196:197], v[196:197], 0, s[78:79]
	global_load_dword v176, v[196:197], off offset:128
	v_lshl_add_u64 v[196:197], v[196:197], 0, s[78:79]
	global_load_dword v177, v[196:197], off offset:128
	v_lshl_add_u64 v[190:191], s[92:93], 0, v[34:35]
	global_load_dword v178, v[190:191], off
	v_lshl_add_u64 v[192:193], v[32:33], 0, s[38:39]
	global_load_dwordx2 v[180:181], v[192:193], off offset:256
	v_lshl_add_u64 v[192:193], v[192:193], 0, s[80:81]
	global_load_dwordx2 v[182:183], v[192:193], off offset:256
	v_lshl_add_u64 v[192:193], v[192:193], 0, s[80:81]
	global_load_dwordx2 v[184:185], v[192:193], off offset:256
	v_lshl_add_u64 v[192:193], v[192:193], 0, s[80:81]
	global_load_dwordx2 v[186:187], v[192:193], off offset:256
	v_lshl_add_u64 v[194:195], v[30:31], 0, s[38:39]
	global_load_dwordx2 v[188:189], v[194:195], off
	s_waitcnt lgkmcnt(0)
	s_barrier
	s_branch .LBB0_403
.LBB0_402:
	s_or_b64 exec, exec, s[42:43]
	s_waitcnt vmcnt(4)
	v_cndmask_b32_e64 v18, v168, 0, s[12:13]
	v_cndmask_b32_e64 v19, v169, 0, s[12:13]
	v_cndmask_b32_e64 v20, v170, 0, s[12:13]
	v_lshlrev_b32_e32 v120, 16, v18
	v_and_b32_e32 v131, 0xffff0000, v18
	v_lshlrev_b32_e32 v121, 16, v19
	v_and_b32_e32 v132, 0xffff0000, v19
	v_lshlrev_b32_e32 v122, 16, v20
	v_and_b32_e32 v133, 0xffff0000, v20
	v_lshlrev_b32_e32 v123, 16, v171
	v_and_b32_e32 v134, 0xffff0000, v171
	v_lshlrev_b32_e32 v124, 16, v172
	v_and_b32_e32 v135, 0xffff0000, v172
	v_lshlrev_b32_e32 v125, 16, v173
	v_and_b32_e32 v136, 0xffff0000, v173
	v_lshlrev_b32_e32 v126, 16, v174
	v_and_b32_e32 v137, 0xffff0000, v174
	v_lshlrev_b32_e32 v127, 16, v175
	v_and_b32_e32 v138, 0xffff0000, v175
	v_lshlrev_b32_e32 v128, 16, v176
	v_and_b32_e32 v139, 0xffff0000, v176
	v_lshlrev_b32_e32 v129, 16, v177
	v_and_b32_e32 v140, 0xffff0000, v177
	v_lshlrev_b32_e32 v130, 16, v178
	v_and_b32_e32 v141, 0xffff0000, v178
	v_mov_b64_e32 v[48:49], v[180:181]
	v_mov_b64_e32 v[56:57], v[182:183]
	v_mov_b64_e32 v[46:47], v[184:185]
	v_mov_b64_e32 v[54:55], v[186:187]
	v_mov_b64_e32 v[50:51], v[188:189]
	v_lshl_add_u64 v[34:35], v[34:35], 0, s[36:37]
	v_lshl_add_u64 v[36:37], v[36:37], 0, s[36:37]
	v_lshl_add_u64 v[38:39], v[38:39], 0, s[36:37]
	v_lshl_add_u64 v[40:41], v[40:41], 0, s[36:37]
	v_lshl_add_u64 v[42:43], v[42:43], 0, s[36:37]
	s_cmpk_eq_i32 s38, 0x600
	s_cbranch_scc1 .Lp2_pf_skip
	s_mov_b32 s76, 0x45c00000
	s_mov_b32 s77, 0
	s_movk_i32 s78, 0x3000
	s_mov_b32 s79, 0
	s_movk_i32 s80, 0x6000
	s_mov_b32 s81, 0
	v_lshl_add_u64 v[190:191], s[92:93], 0, v[42:43]
	v_lshl_add_u64 v[192:193], s[92:93], 0, v[40:41]
	v_lshl_add_u64 v[194:195], s[92:93], 0, v[38:39]
	v_lshl_add_u64 v[196:197], s[92:93], 0, v[36:37]
	global_load_dword v168, v[190:191], off
	global_load_dword v169, v[192:193], off
	global_load_dword v170, v[194:195], off
	v_lshl_add_u64 v[196:197], v[196:197], 0, s[76:77]
	global_load_dword v171, v[196:197], off offset:128
	v_lshl_add_u64 v[196:197], v[196:197], 0, s[78:79]
	global_load_dword v172, v[196:197], off offset:128
	v_lshl_add_u64 v[196:197], v[196:197], 0, s[78:79]
	global_load_dword v173, v[196:197], off offset:128
	v_lshl_add_u64 v[196:197], v[196:197], 0, s[78:79]
	global_load_dword v174, v[196:197], off offset:128
	v_lshl_add_u64 v[196:197], v[196:197], 0, s[78:79]
	global_load_dword v175, v[196:197], off offset:128
	v_lshl_add_u64 v[196:197], v[196:197], 0, s[78:79]
	global_load_dword v176, v[196:197], off offset:128
	v_lshl_add_u64 v[196:197], v[196:197], 0, s[78:79]
	global_load_dword v177, v[196:197], off offset:128
	v_lshl_add_u64 v[190:191], s[92:93], 0, v[34:35]
	global_load_dword v178, v[190:191], off
	v_lshl_add_u64 v[192:193], v[32:33], 0, s[38:39]
	global_load_dwordx2 v[180:181], v[192:193], off offset:512
	v_lshl_add_u64 v[192:193], v[192:193], 0, s[80:81]
	global_load_dwordx2 v[182:183], v[192:193], off offset:512
	v_lshl_add_u64 v[192:193], v[192:193], 0, s[80:81]
	global_load_dwordx2 v[184:185], v[192:193], off offset:512
	v_lshl_add_u64 v[192:193], v[192:193], 0, s[80:81]
	global_load_dwordx2 v[186:187], v[192:193], off offset:512
	v_lshl_add_u64 v[194:195], v[30:31], 0, s[38:39]
	global_load_dwordx2 v[188:189], v[194:195], off offset:256
.Lp2_pf_skip:
	v_mov_b32_e32 v119, s26
	ds_read_b32 v29, v119 offset:5116
	v_add_u32_e32 v112, s26, v87
	ds_read2st64_b32 v[142:143], v112 offset0:2 offset1:18
	v_add_u32_e32 v119, s26, v104
	ds_read_b128 v[144:147], v119 offset:512
	ds_read_b128 v[112:115], v119 offset:4608
	ds_read_b96 v[116:118], v119 offset:528
	ds_read_b96 v[18:20], v119 offset:4624
	s_waitcnt lgkmcnt(0)
	v_sub_f32_e32 v112, v29, v112
	v_sub_f32_e32 v113, v29, v113
	v_sub_f32_e32 v114, v29, v114
	v_sub_f32_e32 v115, v29, v115
	v_sub_f32_e32 v18, v29, v18
	v_sub_f32_e32 v19, v29, v19
	v_sub_f32_e32 v20, v29, v20
	v_sub_f32_e32 v143, v29, v143
	v_mul_f32_e32 v112, 0x3fb8aa3b, v112
	v_mul_f32_e32 v113, 0x3fb8aa3b, v113
	v_mul_f32_e32 v114, 0x3fb8aa3b, v114
	v_mul_f32_e32 v115, 0x3fb8aa3b, v115
	v_mul_f32_e32 v18, 0x3fb8aa3b, v18
	v_mul_f32_e32 v19, 0x3fb8aa3b, v19
	v_mul_f32_e32 v20, 0x3fb8aa3b, v20
	v_mul_f32_e32 v143, 0x3fb8aa3b, v143
	v_exp_f32_e32 v112, v112
	v_exp_f32_e32 v113, v113
	v_exp_f32_e32 v114, v114
	v_exp_f32_e32 v115, v115
	v_exp_f32_e32 v18, v18
	v_exp_f32_e32 v19, v19
	v_exp_f32_e32 v20, v20
	v_exp_f32_e32 v143, v143
	v_mul_f32_e32 v144, v144, v112
	v_mul_f32_e32 v145, v145, v113
	v_mul_f32_e32 v146, v146, v114
	v_mul_f32_e32 v147, v147, v115
	v_mul_f32_e32 v116, v116, v18
	v_mul_f32_e32 v117, v117, v19
	v_mul_f32_e32 v118, v118, v20
	v_mul_f32_e32 v142, v142, v143
	v_fma_f32 v112, v48, v120, v50
	v_fma_f32 v113, v49, v131, v51
	v_fmac_f32_e32 v112, v56, v121
	v_fmac_f32_e32 v113, v57, v132
	v_fmac_f32_e32 v112, v46, v122
	v_fmac_f32_e32 v113, v47, v133
	v_fmac_f32_e32 v112, v54, v123
	v_fmac_f32_e32 v113, v55, v134
	v_mul_f32_e32 v114, 0xbfb8aa3b, v112
	v_mul_f32_e32 v115, 0xbfb8aa3b, v113
	v_exp_f32_e32 v114, v114
	v_exp_f32_e32 v115, v115
	v_add_f32_e32 v114, 1.0, v114
	v_add_f32_e32 v115, 1.0, v115
	v_rcp_f32_e32 v114, v114
	v_rcp_f32_e32 v115, v115
	v_mul_f32_e32 v112, v112, v144
	v_mul_f32_e32 v113, v113, v144
	v_mul_f32_e32 v120, v112, v114
	v_mul_f32_e32 v131, v113, v115
	v_fma_f32 v112, v48, v121, v50
	v_fma_f32 v113, v49, v132, v51
	v_fmac_f32_e32 v112, v56, v122
	v_fmac_f32_e32 v113, v57, v133
	v_fmac_f32_e32 v112, v46, v123
	v_fmac_f32_e32 v113, v47, v134
	v_fmac_f32_e32 v112, v54, v124
	v_fmac_f32_e32 v113, v55, v135
	v_mul_f32_e32 v114, 0xbfb8aa3b, v112
	v_mul_f32_e32 v115, 0xbfb8aa3b, v113
	v_exp_f32_e32 v114, v114
	v_exp_f32_e32 v115, v115
	v_add_f32_e32 v114, 1.0, v114
	v_add_f32_e32 v115, 1.0, v115
	v_rcp_f32_e32 v114, v114
	v_rcp_f32_e32 v115, v115
	v_mul_f32_e32 v112, v112, v145
	v_mul_f32_e32 v113, v113, v145
	v_mul_f32_e32 v121, v112, v114
	v_mul_f32_e32 v132, v113, v115
	v_fma_f32 v112, v48, v122, v50
	v_fma_f32 v113, v49, v133, v51
	v_fmac_f32_e32 v112, v56, v123
	v_fmac_f32_e32 v113, v57, v134
	v_fmac_f32_e32 v112, v46, v124
	v_fmac_f32_e32 v113, v47, v135
	v_fmac_f32_e32 v112, v54, v125
	v_fmac_f32_e32 v113, v55, v136
	v_mul_f32_e32 v114, 0xbfb8aa3b, v112
	v_mul_f32_e32 v115, 0xbfb8aa3b, v113
	v_exp_f32_e32 v114, v114
	v_exp_f32_e32 v115, v115
	v_add_f32_e32 v114, 1.0, v114
	v_add_f32_e32 v115, 1.0, v115
	v_rcp_f32_e32 v114, v114
	v_rcp_f32_e32 v115, v115
	v_mul_f32_e32 v112, v112, v146
	v_mul_f32_e32 v113, v113, v146
	v_mul_f32_e32 v122, v112, v114
	v_mul_f32_e32 v133, v113, v115
	v_fma_f32 v112, v48, v123, v50
	v_fma_f32 v113, v49, v134, v51
	v_fmac_f32_e32 v112, v56, v124
	v_fmac_f32_e32 v113, v57, v135
	v_fmac_f32_e32 v112, v46, v125
	v_fmac_f32_e32 v113, v47, v136
	v_fmac_f32_e32 v112, v54, v126
	v_fmac_f32_e32 v113, v55, v137
	v_mul_f32_e32 v114, 0xbfb8aa3b, v112
	v_mul_f32_e32 v115, 0xbfb8aa3b, v113
	v_exp_f32_e32 v114, v114
	v_exp_f32_e32 v115, v115
	v_add_f32_e32 v114, 1.0, v114
	v_add_f32_e32 v115, 1.0, v115
	v_rcp_f32_e32 v114, v114
	v_rcp_f32_e32 v115, v115
	v_mul_f32_e32 v112, v112, v147
	v_mul_f32_e32 v113, v113, v147
	v_mul_f32_e32 v123, v112, v114
	v_mul_f32_e32 v134, v113, v115
	v_fma_f32 v112, v48, v124, v50
	v_fma_f32 v113, v49, v135, v51
	v_fmac_f32_e32 v112, v56, v125
	v_fmac_f32_e32 v113, v57, v136
	v_fmac_f32_e32 v112, v46, v126
	v_fmac_f32_e32 v113, v47, v137
	v_fmac_f32_e32 v112, v54, v127
	v_fmac_f32_e32 v113, v55, v138
	v_mul_f32_e32 v114, 0xbfb8aa3b, v112
	v_mul_f32_e32 v115, 0xbfb8aa3b, v113
	v_exp_f32_e32 v114, v114
	v_exp_f32_e32 v115, v115
	v_add_f32_e32 v114, 1.0, v114
	v_add_f32_e32 v115, 1.0, v115
	v_rcp_f32_e32 v114, v114
	v_rcp_f32_e32 v115, v115
	v_mul_f32_e32 v112, v112, v116
	v_mul_f32_e32 v113, v113, v116
	v_mul_f32_e32 v124, v112, v114
	v_mul_f32_e32 v135, v113, v115
	v_fma_f32 v112, v48, v125, v50
	v_fma_f32 v113, v49, v136, v51
	v_fmac_f32_e32 v112, v56, v126
	v_fmac_f32_e32 v113, v57, v137
	v_fmac_f32_e32 v112, v46, v127
	v_fmac_f32_e32 v113, v47, v138
	v_fmac_f32_e32 v112, v54, v128
	v_fmac_f32_e32 v113, v55, v139
	v_mul_f32_e32 v114, 0xbfb8aa3b, v112
	v_mul_f32_e32 v115, 0xbfb8aa3b, v113
	v_exp_f32_e32 v114, v114
	v_exp_f32_e32 v115, v115
	v_add_f32_e32 v114, 1.0, v114
	v_add_f32_e32 v115, 1.0, v115
	v_rcp_f32_e32 v114, v114
	v_rcp_f32_e32 v115, v115
	v_mul_f32_e32 v112, v112, v117
	v_mul_f32_e32 v113, v113, v117
	v_mul_f32_e32 v125, v112, v114
	v_mul_f32_e32 v136, v113, v115
	v_fma_f32 v112, v48, v126, v50
	v_fma_f32 v113, v49, v137, v51
	v_fmac_f32_e32 v112, v56, v127
	v_fmac_f32_e32 v113, v57, v138
	v_fmac_f32_e32 v112, v46, v128
	v_fmac_f32_e32 v113, v47, v139
	v_fmac_f32_e32 v112, v54, v129
	v_fmac_f32_e32 v113, v55, v140
	v_mul_f32_e32 v114, 0xbfb8aa3b, v112
	v_mul_f32_e32 v115, 0xbfb8aa3b, v113
	v_exp_f32_e32 v114, v114
	v_exp_f32_e32 v115, v115
	v_add_f32_e32 v114, 1.0, v114
	v_add_f32_e32 v115, 1.0, v115
	v_rcp_f32_e32 v114, v114
	v_rcp_f32_e32 v115, v115
	v_mul_f32_e32 v112, v112, v118
	v_mul_f32_e32 v113, v113, v118
	v_mul_f32_e32 v126, v112, v114
	v_mul_f32_e32 v137, v113, v115
	v_fma_f32 v112, v48, v127, v50
	v_fma_f32 v113, v49, v138, v51
	v_fmac_f32_e32 v112, v56, v128
	v_fmac_f32_e32 v113, v57, v139
	v_fmac_f32_e32 v112, v46, v129
	v_fmac_f32_e32 v113, v47, v140
	v_fmac_f32_e32 v112, v54, v130
	v_fmac_f32_e32 v113, v55, v141
	v_mul_f32_e32 v114, 0xbfb8aa3b, v112
	v_mul_f32_e32 v115, 0xbfb8aa3b, v113
	v_exp_f32_e32 v114, v114
	v_exp_f32_e32 v115, v115
	v_add_f32_e32 v114, 1.0, v114
	v_add_f32_e32 v115, 1.0, v115
	v_rcp_f32_e32 v114, v114
	v_rcp_f32_e32 v115, v115
	v_mul_f32_e32 v112, v112, v142
	v_mul_f32_e32 v113, v113, v142
	v_mul_f32_e32 v127, v112, v114
	v_mul_f32_e32 v138, v113, v115
	s_and_b64 s[40:41], s[40:41], exec
	s_mov_b32 s40, 0xec00
	s_cselect_b32 s40, s40, 0xa800
	s_add_i32 s40, s40, 0
	s_add_i32 s62, s62, 1
	s_add_u32 s38, s38, 0x100
	s_addc_u32 s39, s39, 0
	s_addk_i32 s26, 0x200
	s_add_u32 s58, s58, 4
	s_addc_u32 s61, s61, 0
	v_cvt_pk_bf16_f32 v46, v120, v121
	v_cvt_pk_bf16_f32 v47, v122, v123
	v_cvt_pk_bf16_f32 v48, v124, v125
	v_cvt_pk_bf16_f32 v49, v126, v127
	v_cvt_pk_bf16_f32 v50, v131, v132
	v_cvt_pk_bf16_f32 v51, v133, v134
	v_cvt_pk_bf16_f32 v52, v135, v136
	v_cvt_pk_bf16_f32 v53, v137, v138
	v_add3_u32 v18, s40, v89, v90
	s_mov_b64 s[40:41], 0x4000
	s_cmpk_eq_i32 s38, 0x700
	v_lshl_add_u64 v[44:45], v[44:45], 0, s[40:41]
	ds_write_b128 v18, v[46:49]
	ds_write_b128 v18, v[50:53] offset:272
	s_waitcnt lgkmcnt(0)
	s_barrier
	s_cbranch_scc1 .LBB0_405
.LBB0_403:
	s_bitcmp0_b32 s62, 0
	s_cselect_b64 s[40:41], -1, 0
	s_and_b64 s[42:43], s[40:41], exec
	s_cselect_b32 s42, s52, s53
	v_mov_b32_e32 v52, s26
	v_add3_u32 v53, s42, v92, v93
	ds_read_b32 v52, v52 offset:4604
	ds_read_b128 v[120:123], v53
	ds_read_b128 v[124:127], v53 offset:64
	ds_read_b128 v[128:131], v53 offset:4352
	ds_read_b128 v[132:135], v53 offset:4416
	ds_read_b128 v[136:139], v53 offset:8704
	ds_read_b128 v[140:143], v53 offset:8768
	ds_read_b128 v[144:147], v53 offset:13056
	ds_read_b128 v[148:151], v53 offset:13120
	s_waitcnt lgkmcnt(7)
	v_mfma_f32_16x16x32_bf16 v[120:123], v[14:17], v[120:123], 0
	s_waitcnt lgkmcnt(5)
	v_mfma_f32_16x16x32_bf16 v[128:131], v[14:17], v[128:131], 0
	s_waitcnt lgkmcnt(3)
	v_mfma_f32_16x16x32_bf16 v[136:139], v[14:17], v[136:139], 0
	s_waitcnt lgkmcnt(1)
	v_mfma_f32_16x16x32_bf16 v[144:147], v[14:17], v[144:147], 0
	ds_read_b128 v[152:155], v53 offset:128
	ds_read_b128 v[156:159], v53 offset:4480
	ds_read_b128 v[160:163], v53 offset:8832
	ds_read_b128 v[164:167], v53 offset:13184
	v_mfma_f32_16x16x32_bf16 v[120:123], v[10:13], v[124:127], v[120:123]
	v_mfma_f32_16x16x32_bf16 v[124:127], v[10:13], v[132:135], v[128:131]
	v_mfma_f32_16x16x32_bf16 v[128:131], v[10:13], v[140:143], v[136:139]
	s_waitcnt lgkmcnt(4)
	v_mfma_f32_16x16x32_bf16 v[132:135], v[10:13], v[148:151], v[144:147]
	s_nop 0
	ds_read_b128 v[136:139], v53 offset:192
	ds_read_b128 v[140:143], v53 offset:4544
	ds_read_b128 v[144:147], v53 offset:8896
	ds_read_b128 v[148:151], v53 offset:13248
	s_waitcnt lgkmcnt(7)
	v_mfma_f32_16x16x32_bf16 v[120:123], v[6:9], v[152:155], v[120:123]
	s_waitcnt lgkmcnt(6)
	v_mfma_f32_16x16x32_bf16 v[124:127], v[6:9], v[156:159], v[124:127]
	s_waitcnt lgkmcnt(5)
	v_mfma_f32_16x16x32_bf16 v[128:131], v[6:9], v[160:163], v[128:131]
	s_waitcnt lgkmcnt(4)
	v_mfma_f32_16x16x32_bf16 v[132:135], v[6:9], v[164:167], v[132:135]
	s_waitcnt lgkmcnt(3)
	v_mfma_f32_16x16x32_bf16 v[120:123], v[2:5], v[136:139], v[120:123]
	s_waitcnt lgkmcnt(2)
	v_mfma_f32_16x16x32_bf16 v[124:127], v[2:5], v[140:143], v[124:127]
	s_waitcnt lgkmcnt(1)
	v_mfma_f32_16x16x32_bf16 v[128:131], v[2:5], v[144:147], v[128:131]
	s_waitcnt lgkmcnt(0)
	v_mfma_f32_16x16x32_bf16 v[132:135], v[2:5], v[148:151], v[132:135]
	v_cvt_pk_bf16_f32 v120, v120, v121
	v_cvt_pk_bf16_f32 v121, v122, v123
	s_nop 1
	v_lshl_add_u64 v[122:123], s[92:93], 0, v[44:45]
	s_mov_b32 s42, 0x5e001000
	v_add_co_u32_e32 v136, vcc, s42, v122
	s_mov_b32 s42, 0x5e002000
	s_nop 0
	v_addc_co_u32_e32 v137, vcc, 0, v123, vcc
	global_store_dwordx2 v[136:137], v[120:121], off offset:-4096
	v_cvt_pk_bf16_f32 v120, v124, v125
	v_add_co_u32_e32 v124, vcc, s42, v122
	s_cmp_eq_u32 s84, s62
	s_nop 0
	v_addc_co_u32_e32 v125, vcc, 0, v123, vcc
	v_cvt_pk_bf16_f32 v121, v126, v127
	v_add_co_u32_e32 v122, vcc, 0x5e003000, v122
	s_cselect_b64 s[42:43], -1, 0
	global_store_dwordx2 v[136:137], v[120:121], off
	v_cvt_pk_bf16_f32 v120, v128, v129
	v_cvt_pk_bf16_f32 v121, v130, v131
	v_addc_co_u32_e32 v123, vcc, 0, v123, vcc
	s_and_b64 s[64:65], s[0:1], s[42:43]
	global_store_dwordx2 v[124:125], v[120:121], off
	v_cvt_pk_bf16_f32 v120, v132, v133
	v_cvt_pk_bf16_f32 v121, v134, v135
	global_store_dwordx2 v[122:123], v[120:121], off
	s_and_saveexec_b64 s[42:43], s[64:65]
	s_cbranch_execz .LBB0_402
	v_mul_f32_e32 v52, 0x3fb8aa3b, v52
	v_exp_f32_e32 v52, v52
	s_add_u32 s64, s92, s58
	s_addc_u32 s65, s93, s61
	global_store_dword v21, v52, s[64:65]
	s_branch .LBB0_402

.LBB0_578:
	s_nop 0
	v_lshlrev_b32_e32 v106, 16, v70
	v_and_b32_e32 v108, 0xffff0000, v70
	v_mul_f32_e32 v109, 0xbfb8aa3b, v106
	v_mul_f32_e32 v70, 0xbfb8aa3b, v108
	v_exp_f32_e32 v109, v109
	v_exp_f32_e32 v70, v70
	v_fma_f32 v82, v107, v98, v82
	v_fma_f32 v83, v107, v99, v83
	v_add_f32_e32 v109, 1.0, v109
	v_add_f32_e32 v70, 1.0, v70
	v_rcp_f32_e32 v109, v109
	v_rcp_f32_e32 v70, v70
	v_mul_f32_e32 v82, v82, v106
	v_mul_f32_e32 v83, v83, v108
	v_mul_f32_e32 v82, v82, v109
	v_mul_f32_e32 v83, v83, v70
	v_lshlrev_b32_e32 v106, 16, v71
	v_and_b32_e32 v108, 0xffff0000, v71
	v_mul_f32_e32 v109, 0xbfb8aa3b, v106
	v_mul_f32_e32 v71, 0xbfb8aa3b, v108
	v_exp_f32_e32 v109, v109
	v_exp_f32_e32 v71, v71
	v_fma_f32 v84, v107, v100, v84
	v_fma_f32 v85, v107, v101, v85
	v_add_f32_e32 v109, 1.0, v109
	v_add_f32_e32 v71, 1.0, v71
	v_rcp_f32_e32 v109, v109
	v_rcp_f32_e32 v71, v71
	v_mul_f32_e32 v84, v84, v106
	v_mul_f32_e32 v85, v85, v108
	v_mul_f32_e32 v84, v84, v109
	v_mul_f32_e32 v85, v85, v71
	v_lshlrev_b32_e32 v106, 16, v72
	v_and_b32_e32 v108, 0xffff0000, v72
	v_mul_f32_e32 v109, 0xbfb8aa3b, v106
	v_mul_f32_e32 v72, 0xbfb8aa3b, v108
	v_exp_f32_e32 v109, v109
	v_exp_f32_e32 v72, v72
	v_fma_f32 v78, v107, v94, v78
	v_fma_f32 v94, v107, v95, v79
	v_add_f32_e32 v109, 1.0, v109
	v_add_f32_e32 v72, 1.0, v72
	v_rcp_f32_e32 v109, v109
	v_rcp_f32_e32 v72, v72
	v_mul_f32_e32 v78, v78, v106
	v_mul_f32_e32 v94, v94, v108
	v_mul_f32_e32 v78, v78, v109
	v_mul_f32_e32 v94, v94, v72
	v_lshlrev_b32_e32 v106, 16, v73
	v_and_b32_e32 v108, 0xffff0000, v73
	v_mul_f32_e32 v109, 0xbfb8aa3b, v106
	v_mul_f32_e32 v73, 0xbfb8aa3b, v108
	v_exp_f32_e32 v109, v109
	v_exp_f32_e32 v73, v73
	v_fma_f32 v79, v107, v96, v80
	v_fma_f32 v80, v107, v97, v81
	v_add_f32_e32 v109, 1.0, v109
	v_add_f32_e32 v73, 1.0, v73
	v_rcp_f32_e32 v109, v109
	v_rcp_f32_e32 v73, v73
	v_mul_f32_e32 v79, v79, v106
	v_mul_f32_e32 v80, v80, v108
	v_mul_f32_e32 v79, v79, v109
	v_mul_f32_e32 v80, v80, v73
	v_cvt_pk_bf16_f32 v70, v82, v83
	v_cvt_pk_bf16_f32 v71, v84, v85
	v_cvt_pk_bf16_f32 v72, v78, v94
	v_cvt_pk_bf16_f32 v73, v79, v80
	s_andn2_b64 vcc, exec, s[6:7]
	s_mov_b64 s[6:7], -1
	s_cbranch_vccz .LBB0_596
	s_andn2_b64 vcc, exec, s[6:7]
	s_cbranch_vccz .LBB0_597

.LBB0_598:
	s_cmp_gt_u32 s2, 3
	s_cbranch_scc1 .Lp5_cw2
	s_waitcnt vmcnt(0)
	s_branch .Lp5_cwd
.Lp5_cw2:
	s_waitcnt vmcnt(2)
.Lp5_cwd:
	v_cndmask_b32_e64 v2, v2, 0, s[80:81]
	v_cndmask_b32_e64 v1, v1, 0, s[80:81]
	v_cndmask_b32_e64 v12, v12, 0, s[80:81]
	ds_read_b128 v[96:99], v142
	ds_read_b128 v[70:73], v142 offset:16
	v_lshlrev_b32_e32 v100, 16, v2
	v_and_b32_e32 v128, 0xffff0000, v2
	v_lshlrev_b32_e32 v101, 16, v1
	v_and_b32_e32 v129, 0xffff0000, v1
	v_lshlrev_b32_e32 v102, 16, v12
	v_and_b32_e32 v130, 0xffff0000, v12
	v_lshlrev_b32_e32 v103, 16, v3
	v_and_b32_e32 v131, 0xffff0000, v3
	v_lshlrev_b32_e32 v104, 16, v4
	v_and_b32_e32 v132, 0xffff0000, v4
	v_lshlrev_b32_e32 v105, 16, v5
	v_and_b32_e32 v133, 0xffff0000, v5
	v_lshlrev_b32_e32 v106, 16, v6
	v_and_b32_e32 v134, 0xffff0000, v6
	v_lshlrev_b32_e32 v107, 16, v7
	v_and_b32_e32 v135, 0xffff0000, v7
	v_lshlrev_b32_e32 v108, 16, v8
	v_and_b32_e32 v136, 0xffff0000, v8
	v_lshlrev_b32_e32 v109, 16, v9
	v_and_b32_e32 v137, 0xffff0000, v9
	v_lshlrev_b32_e32 v95, 16, v10
	v_and_b32_e32 v138, 0xffff0000, v10
	v_fma_f32 v148, v176, v100, v184
	v_fma_f32 v149, v177, v128, v185
	v_fmac_f32_e32 v148, v178, v101
	v_fmac_f32_e32 v149, v179, v129
	v_fmac_f32_e32 v148, v180, v102
	v_fmac_f32_e32 v149, v181, v130
	v_fmac_f32_e32 v148, v182, v103
	v_fmac_f32_e32 v149, v183, v131
	v_mul_f32_e32 v150, 0xbfb8aa3b, v148
	v_mul_f32_e32 v151, 0xbfb8aa3b, v149
	v_exp_f32_e32 v150, v150
	v_exp_f32_e32 v151, v151
	v_add_f32_e32 v150, 1.0, v150
	v_add_f32_e32 v151, 1.0, v151
	v_rcp_f32_e32 v150, v150
	v_rcp_f32_e32 v151, v151
	s_waitcnt lgkmcnt(0)
	v_mul_f32_e32 v148, v148, v150
	v_mul_f32_e32 v149, v149, v151
	v_mul_f32_e32 v100, v148, v96
	v_mul_f32_e32 v128, v149, v96
	v_fma_f32 v148, v176, v101, v184
	v_fma_f32 v149, v177, v129, v185
	v_fmac_f32_e32 v148, v178, v102
	v_fmac_f32_e32 v149, v179, v130
	v_fmac_f32_e32 v148, v180, v103
	v_fmac_f32_e32 v149, v181, v131
	v_fmac_f32_e32 v148, v182, v104
	v_fmac_f32_e32 v149, v183, v132
	v_mul_f32_e32 v150, 0xbfb8aa3b, v148
	v_mul_f32_e32 v151, 0xbfb8aa3b, v149
	v_exp_f32_e32 v150, v150
	v_exp_f32_e32 v151, v151
	v_add_f32_e32 v150, 1.0, v150
	v_add_f32_e32 v151, 1.0, v151
	v_rcp_f32_e32 v150, v150
	v_rcp_f32_e32 v151, v151
	v_mul_f32_e32 v148, v148, v150
	v_mul_f32_e32 v149, v149, v151
	v_mul_f32_e32 v101, v148, v97
	v_mul_f32_e32 v129, v149, v97
	v_fma_f32 v148, v176, v102, v184
	v_fma_f32 v149, v177, v130, v185
	v_fmac_f32_e32 v148, v178, v103
	v_fmac_f32_e32 v149, v179, v131
	v_fmac_f32_e32 v148, v180, v104
	v_fmac_f32_e32 v149, v181, v132
	v_fmac_f32_e32 v148, v182, v105
	v_fmac_f32_e32 v149, v183, v133
	v_mul_f32_e32 v150, 0xbfb8aa3b, v148
	v_mul_f32_e32 v151, 0xbfb8aa3b, v149
	v_exp_f32_e32 v150, v150
	v_exp_f32_e32 v151, v151
	v_add_f32_e32 v150, 1.0, v150
	v_add_f32_e32 v151, 1.0, v151
	v_rcp_f32_e32 v150, v150
	v_rcp_f32_e32 v151, v151
	v_mul_f32_e32 v148, v148, v150
	v_mul_f32_e32 v149, v149, v151
	v_mul_f32_e32 v102, v148, v98
	v_mul_f32_e32 v130, v149, v98
	v_fma_f32 v148, v176, v103, v184
	v_fma_f32 v149, v177, v131, v185
	v_fmac_f32_e32 v148, v178, v104
	v_fmac_f32_e32 v149, v179, v132
	v_fmac_f32_e32 v148, v180, v105
	v_fmac_f32_e32 v149, v181, v133
	v_fmac_f32_e32 v148, v182, v106
	v_fmac_f32_e32 v149, v183, v134
	v_mul_f32_e32 v150, 0xbfb8aa3b, v148
	v_mul_f32_e32 v151, 0xbfb8aa3b, v149
	v_exp_f32_e32 v150, v150
	v_exp_f32_e32 v151, v151
	v_add_f32_e32 v150, 1.0, v150
	v_add_f32_e32 v151, 1.0, v151
	v_rcp_f32_e32 v150, v150
	v_rcp_f32_e32 v151, v151
	v_mul_f32_e32 v148, v148, v150
	v_mul_f32_e32 v149, v149, v151
	v_mul_f32_e32 v103, v148, v99
	v_mul_f32_e32 v131, v149, v99
	v_fma_f32 v148, v176, v104, v184
	v_fma_f32 v149, v177, v132, v185
	v_fmac_f32_e32 v148, v178, v105
	v_fmac_f32_e32 v149, v179, v133
	v_fmac_f32_e32 v148, v180, v106
	v_fmac_f32_e32 v149, v181, v134
	v_fmac_f32_e32 v148, v182, v107
	v_fmac_f32_e32 v149, v183, v135
	v_mul_f32_e32 v150, 0xbfb8aa3b, v148
	v_mul_f32_e32 v151, 0xbfb8aa3b, v149
	v_exp_f32_e32 v150, v150
	v_exp_f32_e32 v151, v151
	v_add_f32_e32 v150, 1.0, v150
	v_add_f32_e32 v151, 1.0, v151
	v_rcp_f32_e32 v150, v150
	v_rcp_f32_e32 v151, v151
	v_mul_f32_e32 v148, v148, v150
	v_mul_f32_e32 v149, v149, v151
	v_mul_f32_e32 v104, v148, v70
	v_mul_f32_e32 v132, v149, v70
	v_fma_f32 v148, v176, v105, v184
	v_fma_f32 v149, v177, v133, v185
	v_fmac_f32_e32 v148, v178, v106
	v_fmac_f32_e32 v149, v179, v134
	v_fmac_f32_e32 v148, v180, v107
	v_fmac_f32_e32 v149, v181, v135
	v_fmac_f32_e32 v148, v182, v108
	v_fmac_f32_e32 v149, v183, v136
	v_mul_f32_e32 v150, 0xbfb8aa3b, v148
	v_mul_f32_e32 v151, 0xbfb8aa3b, v149
	v_exp_f32_e32 v150, v150
	v_exp_f32_e32 v151, v151
	v_add_f32_e32 v150, 1.0, v150
	v_add_f32_e32 v151, 1.0, v151
	v_rcp_f32_e32 v150, v150
	v_rcp_f32_e32 v151, v151
	v_mul_f32_e32 v148, v148, v150
	v_mul_f32_e32 v149, v149, v151
	v_mul_f32_e32 v105, v148, v71
	v_mul_f32_e32 v133, v149, v71
	v_fma_f32 v148, v176, v106, v184
	v_fma_f32 v149, v177, v134, v185
	v_fmac_f32_e32 v148, v178, v107
	v_fmac_f32_e32 v149, v179, v135
	v_fmac_f32_e32 v148, v180, v108
	v_fmac_f32_e32 v149, v181, v136
	v_fmac_f32_e32 v148, v182, v109
	v_fmac_f32_e32 v149, v183, v137
	v_mul_f32_e32 v150, 0xbfb8aa3b, v148
	v_mul_f32_e32 v151, 0xbfb8aa3b, v149
	v_exp_f32_e32 v150, v150
	v_exp_f32_e32 v151, v151
	v_add_f32_e32 v150, 1.0, v150
	v_add_f32_e32 v151, 1.0, v151
	v_rcp_f32_e32 v150, v150
	v_rcp_f32_e32 v151, v151
	v_mul_f32_e32 v148, v148, v150
	v_mul_f32_e32 v149, v149, v151
	v_mul_f32_e32 v106, v148, v72
	v_mul_f32_e32 v134, v149, v72
	v_fma_f32 v148, v176, v107, v184
	v_fma_f32 v149, v177, v135, v185
	v_fmac_f32_e32 v148, v178, v108
	v_fmac_f32_e32 v149, v179, v136
	v_fmac_f32_e32 v148, v180, v109
	v_fmac_f32_e32 v149, v181, v137
	v_fmac_f32_e32 v148, v182, v95
	v_fmac_f32_e32 v149, v183, v138
	v_mul_f32_e32 v150, 0xbfb8aa3b, v148
	v_mul_f32_e32 v151, 0xbfb8aa3b, v149
	v_exp_f32_e32 v150, v150
	v_exp_f32_e32 v151, v151
	v_add_f32_e32 v150, 1.0, v150
	v_add_f32_e32 v151, 1.0, v151
	v_rcp_f32_e32 v150, v150
	v_rcp_f32_e32 v151, v151
	v_mul_f32_e32 v148, v148, v150
	v_mul_f32_e32 v149, v149, v151
	v_mul_f32_e32 v107, v148, v73
	v_mul_f32_e32 v135, v149, v73
	s_and_b64 s[4:5], s[90:91], exec
	s_cselect_b32 s4, s51, s33
	s_add_i32 s6, 0, 0xec00
	v_cvt_pk_bf16_f32 v70, v100, v101
	v_cvt_pk_bf16_f32 v71, v102, v103
	v_cvt_pk_bf16_f32 v72, v104, v105
	v_cvt_pk_bf16_f32 v73, v106, v107
	v_cvt_pk_bf16_f32 v74, v128, v129
	v_cvt_pk_bf16_f32 v75, v130, v131
	v_cvt_pk_bf16_f32 v76, v132, v133
	v_cvt_pk_bf16_f32 v77, v134, v135
	v_add3_u32 v81, s4, v225, v226
	s_and_b64 s[4:5], s[90:91], exec
	s_cselect_b32 s4, s6, s10
	ds_write_b128 v81, v[70:73]
	ds_write_b128 v81, v[74:77] offset:272
	v_add3_u32 v70, s4, v228, v158
	ds_write_b128 v70, v[14:17]
	v_add3_u32 v70, s4, v230, v158
	ds_write_b128 v70, v[18:21]
	s_branch .LBB0_564
